# speedup vs baseline: 1.0344x; 1.0344x over previous
.Lat_spec_ok:
	v_and_b32_e32 v31, 7, v0
	v_bitop3_b32 v33, v10, v0, 7 bitop3:0x78
	v_lshlrev_b32_e32 v1, 7, v1
	v_mbcnt_lo_u32_b32 v34, -1, 0
	v_lshlrev_b32_e32 v89, 4, v33
	v_bitop3_b32 v31, v10, v31, 4 bitop3:0x36
	v_xor_b32_e32 v33, v13, v0
	v_mov_b32_e32 v13, v12
	v_lshlrev_b32_e32 v87, 4, v11
	s_movk_i32 s1, 0x70
	v_lshlrev_b32_e32 v98, 2, v10
	v_mov_b32_e32 v10, v12
	v_mov_b32_e32 v11, v12
	v_mbcnt_hi_u32_b32 v0, -1, v34
	v_lshl_or_b32 v91, v31, 4, v1
	v_lshlrev_b32_e32 v31, 4, v33
	v_mov_b64_e32 v[36:37], v[12:13]
	v_mov_b64_e32 v[40:41], v[12:13]
	v_mov_b64_e32 v[44:45], v[12:13]
	v_mov_b64_e32 v[48:49], v[12:13]
	v_mov_b64_e32 v[52:53], v[12:13]
	s_mov_b32 s17, 0
	v_mov_b64_e32 v[100:101], 0
	s_mov_b64 s[14:15], -1
	s_mov_b32 s5, 0xff800000
	s_mov_b32 s7, 0x41000000
	s_mov_b32 s12, 0x3c003c00
	v_mov_b32_e32 v30, 0x3c003c00
	v_mov_b32_e32 v114, v30
	v_mov_b32_e32 v115, v30
	v_mov_b32_e32 v116, v30
	v_mov_b32_e32 v117, v30
	v_mov_b32_e32 v54, v12
	v_mov_b64_e32 v[34:35], v[10:11]
	v_mov_b64_e32 v[38:39], v[10:11]
	v_mov_b64_e32 v[42:43], v[10:11]
	v_mov_b64_e32 v[46:47], v[10:11]
	v_mov_b64_e32 v[50:51], v[10:11]
	v_and_or_b32 v99, v31, s1, v32
	s_mov_b32 s9, 0
	s_waitcnt vmcnt(3)
	ds_write_b128 v99, v[22:25]
	ds_write_b128 v90, v[14:17] offset:8192
	s_waitcnt vmcnt(2)
	ds_write_b128 v99, v[18:21] offset:4096
	s_waitcnt vmcnt(1)
	ds_write_b128 v90, v[26:29] offset:12288
	s_waitcnt vmcnt(0)
	s_cmp_gt_i32 s11, 3
	s_cbranch_scc0 .LBB1_20

.LBB1_27:
	s_waitcnt lgkmcnt(0)
	s_barrier
	s_lshl_b32 s10, s9, 14
	s_lshl_b32 s13, 1, s0
	s_and_b32 s0, s13, s4
	v_or_b32_e32 v10, s10, v89
	s_cmp_eq_u32 s0, 0
	v_mov_b32_e32 v55, v54
	v_mov_b32_e32 v56, v54
	v_mov_b32_e32 v57, v54
	v_add_u32_e32 v106, v10, v1
	v_add_u32_e32 v105, s10, v91
	s_cbranch_scc1 .LBB1_32
	ds_read_b128 v[58:61], v106
	ds_read_b128 v[62:65], v105
	v_lshrrev_b64 v[10:11], v98, v[102:103]
	v_bfe_i32 v13, v10, 1, 1
	v_bfe_i32 v31, v10, 2, 1
	s_waitcnt lgkmcnt(1)
	v_mfma_f32_16x16x32_f16 v[58:61], v[58:61], v[2:5], v[54:57]
	v_bfe_i32 v32, v10, 3, 1
	v_bfe_i32 v11, v10, 0, 1
	s_waitcnt lgkmcnt(0)
	v_mfma_f32_16x16x32_f16 v[58:61], v[62:65], v[6:9], v[58:61]
	s_nop 7
	v_bitop3_b32 v10, v59, s5, v13 bitop3:0xe4
	v_bitop3_b32 v31, v60, s5, v31 bitop3:0xe4
	v_bitop3_b32 v13, v61, s5, v32 bitop3:0xe4
	v_max_f32_e32 v32, v13, v13
	v_max_f32_e32 v33, v31, v31
	v_bitop3_b32 v11, v58, s5, v11 bitop3:0xe4
	v_max_f32_e32 v32, v33, v32
	v_max3_f32 v32, v11, v10, v32
	v_cmp_lt_f32_e32 vcc, s7, v32
	s_or_b64 s[0:1], s[14:15], vcc
	s_cbranch_scc0 .LBB1_35
	v_and_b32_e32 v58, 64, v0
	v_xor_b32_e32 v33, 16, v0
	v_add_u32_e32 v58, 64, v58
	v_cmp_lt_i32_e32 vcc, v33, v58
	s_mov_b64 s[22:23], 0
	s_nop 0
	v_cndmask_b32_e32 v33, v0, v33, vcc
	v_lshlrev_b32_e32 v33, 2, v33
	ds_bpermute_b32 v33, v33, v32
	v_max_f32_e32 v32, v32, v32
	s_waitcnt lgkmcnt(0)
	v_max_f32_e32 v33, v33, v33
	v_max_f32_e32 v32, v32, v33
	v_mov_b32_e32 v33, v32
	s_nop 1
	v_permlane32_swap_b32_e32 v32, v33
	v_max_f32_e32 v33, v33, v33
	v_max_f32_e32 v32, v32, v32
	v_max_f32_e32 v32, v32, v33
	v_cmp_nlg_f32_e32 vcc, s5, v32
	v_cmp_lg_f32_e64 s[0:1], s5, v32
	s_and_saveexec_b64 s[24:25], s[0:1]
	v_cmp_lt_f32_e64 s[0:1], s7, v32
	s_or_b64 s[0:1], s[14:15], s[0:1]
	s_and_b64 s[22:23], s[0:1], exec
	s_or_b64 exec, exec, s[24:25]
	v_exp_f32_e64 v33, -v32
	v_cndmask_b32_e64 v32, 0, v32, s[22:23]
	v_sub_f32_e32 v11, v11, v32
	v_sub_f32_e32 v10, v10, v32
	v_cndmask_b32_e64 v33, v33, 1.0, s[14:15]
	v_cndmask_b32_e64 v66, 1.0, v33, s[22:23]
	v_pk_mul_f32 v[60:61], v[48:49], v[66:67] op_sel_hi:[1,0]
	v_pk_mul_f32 v[58:59], v[46:47], v[66:67] op_sel_hi:[1,0]
	v_pk_mul_f32 v[64:65], v[66:67], v[44:45] op_sel_hi:[0,1]
	v_pk_mul_f32 v[62:63], v[66:67], v[42:43] op_sel_hi:[0,1]
	v_pk_mul_f32 v[80:81], v[66:67], v[40:41] op_sel_hi:[0,1]
	v_pk_mul_f32 v[78:79], v[66:67], v[38:39] op_sel_hi:[0,1]
	v_pk_mul_f32 v[84:85], v[66:67], v[36:37] op_sel_hi:[0,1]
	v_pk_mul_f32 v[82:83], v[66:67], v[34:35] op_sel_hi:[0,1]
	v_pk_mul_f32 v[68:69], v[52:53], v[66:67] op_sel_hi:[1,0]
	v_pk_mul_f32 v[66:67], v[50:51], v[66:67] op_sel_hi:[1,0]
	v_sub_f32_e32 v31, v31, v32
	v_sub_f32_e32 v13, v13, v32
	v_sub_f32_e32 v104, v54, v32
	s_and_b64 s[0:1], s[14:15], vcc
	s_branch .LBB1_36

.LBB1_36:
	v_add_u32_e32 v107, s10, v87
	v_exp_f32_e32 v31, v31
	v_exp_f32_e32 v13, v13
	ds_read_b128 v[70:73], v107 offset:8192
	v_exp_f32_e32 v74, v11
	v_exp_f32_e32 v10, v10
	v_cvt_pkrtz_f16_f32 v11, v31, v13
	v_cvt_pkrtz_f16_f32 v10, v74, v10
	v_mov_b32_e32 v13, v12
	ds_read_b128 v[108:111], v107 offset:14336
	s_nop 0
	v_mfma_f32_16x16x32_f16 v[74:77], v[114:117], v[10:13], v[66:69]
	s_nop 2
	ds_read_b128 v[66:69], v107 offset:10240
	s_waitcnt lgkmcnt(2)
	v_mfma_f32_16x16x32_f16 v[70:73], v[70:73], v[10:13], v[58:61]
	s_nop 2
	ds_read_b128 v[58:61], v107 offset:12288
	s_waitcnt lgkmcnt(1)
	v_mfma_f32_16x16x32_f16 v[66:69], v[66:69], v[10:13], v[62:65]
	s_waitcnt lgkmcnt(0)
	v_mfma_f32_16x16x32_f16 v[62:65], v[58:61], v[10:13], v[78:81]
	v_mfma_f32_16x16x32_f16 v[58:61], v[108:111], v[10:13], v[82:85]
	s_branch .LBB1_33

.LBB1_39:
	s_nop 0
	v_max3_f32 v10, v70, v71, v68
	v_max_f32_e32 v10, v10, v69
	v_max3_f32 v10, v10, v64, v65
	v_max3_f32 v10, v10, v66, v67
	v_max3_f32 v10, v10, v60, v61
	v_max3_f32 v10, v10, v62, v63
	v_max3_f32 v10, v10, v56, v57
	v_max3_f32 v10, v10, v58, v59
	v_cmp_lt_f32_e32 vcc, s7, v10
	s_or_b64 s[0:1], s[14:15], vcc
	s_cbranch_scc0 .LBB1_43
	v_and_b32_e32 v13, 64, v0
	v_xor_b32_e32 v11, 16, v0
	v_add_u32_e32 v13, 64, v13
	v_cmp_lt_i32_e32 vcc, v11, v13
	s_mov_b64 s[22:23], 0
	s_nop 0
	v_cndmask_b32_e32 v11, v0, v11, vcc
	v_lshlrev_b32_e32 v11, 2, v11
	ds_bpermute_b32 v11, v11, v10
	v_max_f32_e32 v10, v10, v10
	s_waitcnt lgkmcnt(0)
	v_max_f32_e32 v11, v11, v11
	v_max_f32_e32 v10, v10, v11
	v_mov_b32_e32 v11, v10
	s_nop 1
	v_permlane32_swap_b32_e32 v10, v11
	v_max_f32_e32 v11, v11, v11
	v_max_f32_e32 v10, v10, v10
	v_max_f32_e32 v10, v10, v11
	v_cmp_nlg_f32_e32 vcc, s5, v10
	v_cmp_lg_f32_e64 s[0:1], s5, v10
	s_and_saveexec_b64 s[24:25], s[0:1]
	v_cmp_lt_f32_e64 s[0:1], s7, v10
	s_or_b64 s[0:1], s[14:15], s[0:1]
	s_and_b64 s[22:23], s[0:1], exec
	s_or_b64 exec, exec, s[24:25]
	v_exp_f32_e64 v11, -v10
	v_cndmask_b32_e64 v10, 0, v10, s[22:23]
	v_sub_f32_e32 v104, v54, v10
	s_and_b64 s[0:1], s[14:15], vcc
	v_cndmask_b32_e64 v11, v11, 1.0, s[14:15]
	v_cndmask_b32_e64 v32, 1.0, v11, s[22:23]
	v_pk_mul_f32 v[48:49], v[48:49], v[32:33] op_sel_hi:[1,0]
	v_pk_mul_f32 v[46:47], v[46:47], v[32:33] op_sel_hi:[1,0]
	v_pk_mul_f32 v[44:45], v[32:33], v[44:45] op_sel_hi:[0,1]
	v_pk_mul_f32 v[42:43], v[32:33], v[42:43] op_sel_hi:[0,1]
	v_pk_mul_f32 v[40:41], v[32:33], v[40:41] op_sel_hi:[0,1]
	v_pk_mul_f32 v[38:39], v[32:33], v[38:39] op_sel_hi:[0,1]
	v_pk_mul_f32 v[36:37], v[32:33], v[36:37] op_sel_hi:[0,1]
	v_pk_mul_f32 v[34:35], v[32:33], v[34:35] op_sel_hi:[0,1]
	v_pk_mul_f32 v[52:53], v[52:53], v[32:33] op_sel_hi:[1,0]
	v_pk_mul_f32 v[50:51], v[50:51], v[32:33] op_sel_hi:[1,0]
	v_pk_add_f32 v[68:69], v[68:69], v[10:11] op_sel_hi:[1,0] neg_lo:[0,1] neg_hi:[0,1]
	v_pk_add_f32 v[70:71], v[70:71], v[10:11] op_sel_hi:[1,0] neg_lo:[0,1] neg_hi:[0,1]
	v_pk_add_f32 v[64:65], v[64:65], v[10:11] op_sel_hi:[1,0] neg_lo:[0,1] neg_hi:[0,1]
	v_pk_add_f32 v[66:67], v[66:67], v[10:11] op_sel_hi:[1,0] neg_lo:[0,1] neg_hi:[0,1]
	v_pk_add_f32 v[60:61], v[60:61], v[10:11] op_sel_hi:[1,0] neg_lo:[0,1] neg_hi:[0,1]
	v_pk_add_f32 v[62:63], v[62:63], v[10:11] op_sel_hi:[1,0] neg_lo:[0,1] neg_hi:[0,1]
	v_pk_add_f32 v[56:57], v[56:57], v[10:11] op_sel_hi:[1,0] neg_lo:[0,1] neg_hi:[0,1]
	v_pk_add_f32 v[58:59], v[58:59], v[10:11] op_sel_hi:[1,0] neg_lo:[0,1] neg_hi:[0,1]
	s_branch .LBB1_44

.LBB1_44:
	v_exp_f32_e32 v10, v68
	v_exp_f32_e32 v11, v69
	v_exp_f32_e32 v32, v64
	v_exp_f32_e32 v13, v70
	v_exp_f32_e32 v31, v71
	v_cvt_pkrtz_f16_f32 v64, v10, v11
	v_add_u32_e32 v10, s10, v87
	ds_read_b128 v[72:75], v10 offset:8192
	ds_read_b128 v[76:79], v10 offset:10240
	v_exp_f32_e32 v33, v65
	v_exp_f32_e32 v54, v66
	v_exp_f32_e32 v55, v67
	ds_read_b128 v[80:83], v10 offset:12288
	ds_read_b128 v[106:109], v10 offset:9216
	v_cvt_pkrtz_f16_f32 v65, v13, v31
	v_cvt_pkrtz_f16_f32 v67, v54, v55
	v_cvt_pkrtz_f16_f32 v66, v32, v33
	v_exp_f32_e32 v84, v60
	v_exp_f32_e32 v85, v61
	v_exp_f32_e32 v11, v62
	s_waitcnt lgkmcnt(3)
	v_mfma_f32_16x16x32_f16 v[46:49], v[72:75], v[64:67], v[46:49]
	v_exp_f32_e32 v13, v63
	ds_read_b128 v[60:63], v10 offset:14336
	ds_read_b128 v[110:113], v10 offset:11264
	v_exp_f32_e32 v31, v56
	s_waitcnt lgkmcnt(4)
	v_mfma_f32_16x16x32_f16 v[42:45], v[76:79], v[64:67], v[42:45]
	v_exp_f32_e32 v72, v57
	ds_read_b128 v[54:57], v10 offset:13312
	v_exp_f32_e32 v73, v58
	s_waitcnt lgkmcnt(4)
	v_mfma_f32_16x16x32_f16 v[38:41], v[80:83], v[64:67], v[38:41]
	ds_read_b128 v[78:81], v10 offset:15360
	v_exp_f32_e32 v74, v59
	v_cvt_pkrtz_f16_f32 v58, v84, v85
	v_mfma_f32_16x16x32_f16 v[50:53], v[114:117], v[64:67], v[50:53]
	v_cvt_pkrtz_f16_f32 v59, v11, v13
	s_waitcnt lgkmcnt(3)
	v_mfma_f32_16x16x32_f16 v[34:37], v[60:63], v[64:67], v[34:37]
	v_cvt_pkrtz_f16_f32 v61, v73, v74
	v_cvt_pkrtz_f16_f32 v60, v31, v72
	s_nop 1
	v_mfma_f32_16x16x32_f16 v[50:53], v[114:117], v[58:61], v[50:53]
	v_mfma_f32_16x16x32_f16 v[46:49], v[106:109], v[58:61], v[46:49]
	s_waitcnt lgkmcnt(2)
	v_mfma_f32_16x16x32_f16 v[42:45], v[110:113], v[58:61], v[42:45]
	s_waitcnt lgkmcnt(1)
	v_mfma_f32_16x16x32_f16 v[38:41], v[54:57], v[58:61], v[38:41]
	s_waitcnt lgkmcnt(0)
	v_mfma_f32_16x16x32_f16 v[34:37], v[78:81], v[58:61], v[34:37]
	s_andn2_b64 vcc, exec, s[18:19]
	s_cbranch_vccnz .Lat_exit4
	s_xor_b32 s9, s9, 1
	s_lshl_b32 s10, s9, 14
	s_waitcnt vmcnt(0)
	v_or_b32_e32 v10, s10, v99
	v_mov_b64_e32 v[102:103], v[100:101]
	v_or_b32_e32 v11, s10, v90
	ds_write_b128 v10, v[22:25]
	ds_write_b128 v11, v[14:17] offset:8192
	ds_write_b128 v10, v[18:21] offset:4096
	ds_write_b128 v11, v[26:29] offset:12288
	s_mov_b64 s[14:15], s[0:1]
	s_mov_b32 s0, s16
	v_mov_b32_e32 v54, v104
	s_cmp_gt_i32 s11, 3
	s_cbranch_scc1 .LBB1_17
	s_branch .LBB1_20

	.amdhsa_kernel _Z11attn_kernelPKDF16_S0_S0_PKyPKiPDF16_
		.amdhsa_group_segment_fixed_size 36864
		.amdhsa_private_segment_fixed_size 0
		.amdhsa_kernarg_size 48
		.amdhsa_user_sgpr_count 2
		.amdhsa_user_sgpr_dispatch_ptr 0
		.amdhsa_user_sgpr_queue_ptr 0
		.amdhsa_user_sgpr_kernarg_segment_ptr 1
		.amdhsa_user_sgpr_dispatch_id 0
		.amdhsa_user_sgpr_kernarg_preload_length 0
		.amdhsa_user_sgpr_kernarg_preload_offset 0
		.amdhsa_user_sgpr_private_segment_size 0
		.amdhsa_uses_dynamic_stack 0
		.amdhsa_enable_private_segment 0
		.amdhsa_system_sgpr_workgroup_id_x 1
		.amdhsa_system_sgpr_workgroup_id_y 0
		.amdhsa_system_sgpr_workgroup_id_z 0
		.amdhsa_system_sgpr_workgroup_info 0
		.amdhsa_system_vgpr_workitem_id 0
		.amdhsa_next_free_vgpr 118
		.amdhsa_next_free_sgpr 96
		.amdhsa_accum_offset 120
		.amdhsa_reserve_vcc 1
		.amdhsa_float_round_mode_32 0
		.amdhsa_float_round_mode_16_64 0
		.amdhsa_float_denorm_mode_32 3
		.amdhsa_float_denorm_mode_16_64 3
		.amdhsa_dx10_clamp 1
		.amdhsa_ieee_mode 1
		.amdhsa_fp16_overflow 0
		.amdhsa_tg_split 0
		.amdhsa_exception_fp_ieee_invalid_op 0
		.amdhsa_exception_fp_denorm_src 0
		.amdhsa_exception_fp_ieee_div_zero 0
		.amdhsa_exception_fp_ieee_overflow 0
		.amdhsa_exception_fp_ieee_underflow 0
		.amdhsa_exception_fp_ieee_inexact 0
		.amdhsa_exception_int_div_zero 0
	.end_amdhsa_kernel

amdhsa.kernels:
  - .agpr_count:     0
    .args:
      - .actual_access:  read_only
        .address_space:  global
        .offset:         0
        .size:           8
        .value_kind:     global_buffer
      - .actual_access:  read_only
        .address_space:  global
        .offset:         8
        .size:           8
        .value_kind:     global_buffer
      - .actual_access:  read_only
        .address_space:  global
        .offset:         16
        .size:           8
        .value_kind:     global_buffer
      - .actual_access:  read_only
        .address_space:  global
        .offset:         24
        .size:           8
        .value_kind:     global_buffer
      - .actual_access:  read_only
        .address_space:  global
        .offset:         32
        .size:           8
        .value_kind:     global_buffer
      - .actual_access:  read_only
        .address_space:  global
        .offset:         40
        .size:           8
        .value_kind:     global_buffer
      - .actual_access:  write_only
        .address_space:  global
        .offset:         48
        .size:           8
        .value_kind:     global_buffer
      - .actual_access:  write_only
        .address_space:  global
        .offset:         56
        .size:           8
        .value_kind:     global_buffer
      - .actual_access:  write_only
        .address_space:  global
        .offset:         64
        .size:           8
        .value_kind:     global_buffer
      - .actual_access:  write_only
        .address_space:  global
        .offset:         72
        .size:           8
        .value_kind:     global_buffer
      - .actual_access:  write_only
        .address_space:  global
        .offset:         80
        .size:           8
        .value_kind:     global_buffer
    .group_segment_fixed_size: 16640
    .kernarg_segment_align: 8
    .kernarg_segment_size: 88
    .language:       OpenCL C
    .language_version:
      - 2
      - 0
    .max_flat_workgroup_size: 256
    .name:           _Z11prep_kernelPKfS0_S0_S0_S0_PKiPDF16_S3_S3_PyPi
    .private_segment_fixed_size: 0
    .sgpr_count:     54
    .sgpr_spill_count: 0
    .symbol:         _Z11prep_kernelPKfS0_S0_S0_S0_PKiPDF16_S3_S3_PyPi.kd
    .uniform_work_group_size: 1
    .uses_dynamic_stack: false
    .vgpr_count:     46
    .vgpr_spill_count: 0
    .wavefront_size: 64
  - .agpr_count:     0
    .args:
      - .actual_access:  read_only
        .address_space:  global
        .offset:         0
        .size:           8
        .value_kind:     global_buffer
      - .actual_access:  read_only
        .address_space:  global
        .offset:         8
        .size:           8
        .value_kind:     global_buffer
      - .actual_access:  read_only
        .address_space:  global
        .offset:         16
        .size:           8
        .value_kind:     global_buffer
      - .actual_access:  read_only
        .address_space:  global
        .offset:         24
        .size:           8
        .value_kind:     global_buffer
      - .actual_access:  read_only
        .address_space:  global
        .offset:         32
        .size:           8
        .value_kind:     global_buffer
      - .actual_access:  write_only
        .address_space:  global
        .offset:         40
        .size:           8
        .value_kind:     global_buffer
    .group_segment_fixed_size: 36864
    .kernarg_segment_align: 8
    .kernarg_segment_size: 48
    .language:       OpenCL C
    .language_version:
      - 2
      - 0
    .max_flat_workgroup_size: 256
    .name:           _Z11attn_kernelPKDF16_S0_S0_PKyPKiPDF16_
    .private_segment_fixed_size: 0
    .sgpr_count:     32
    .sgpr_spill_count: 0
    .symbol:         _Z11attn_kernelPKDF16_S0_S0_PKyPKiPDF16_.kd
    .uniform_work_group_size: 1
    .uses_dynamic_stack: false
    .vgpr_count:     118
    .vgpr_spill_count: 0
    .wavefront_size: 64
  - .agpr_count:     0
    .args:
      - .address_space:  global
        .offset:         0
        .size:           8
        .value_kind:     global_buffer
      - .address_space:  global
        .offset:         8
        .size:           8
        .value_kind:     global_buffer
      - .actual_access:  read_only
        .address_space:  global
        .offset:         16
        .size:           8
        .value_kind:     global_buffer
      - .actual_access:  read_only
        .address_space:  global
        .offset:         24
        .size:           8
        .value_kind:     global_buffer
      - .actual_access:  read_only
        .address_space:  global
        .offset:         32
        .size:           8
        .value_kind:     global_buffer
      - .actual_access:  read_only
        .address_space:  global
        .offset:         40
        .size:           8
        .value_kind:     global_buffer
      - .actual_access:  write_only
        .address_space:  global
        .offset:         48
        .size:           8
        .value_kind:     global_buffer
      - .actual_access:  write_only
        .address_space:  global
        .offset:         56
        .size:           8
        .value_kind:     global_buffer
      - .actual_access:  write_only
        .address_space:  global
        .offset:         64
        .size:           8
        .value_kind:     global_buffer
    .group_segment_fixed_size: 114688
    .kernarg_segment_align: 8
    .kernarg_segment_size: 72
    .language:       OpenCL C
    .language_version:
      - 2
      - 0
    .max_flat_workgroup_size: 512
    .name:           _Z9gemm_gldsILi256ELi192ELi4ELi2ELi2ELi4ELi8ELi0ELi4096ELi3072ELi1024EEvPKDF16_S1_PfPKfS4_PKiPDF16_S7_S7_
    .private_segment_fixed_size: 0
    .sgpr_count:     29
    .sgpr_spill_count: 0
    .symbol:         _Z9gemm_gldsILi256ELi192ELi4ELi2ELi2ELi4ELi8ELi0ELi4096ELi3072ELi1024EEvPKDF16_S1_PfPKfS4_PKiPDF16_S7_S7_.kd
    .uniform_work_group_size: 1
    .uses_dynamic_stack: false
    .vgpr_count:     214
    .vgpr_spill_count: 0
    .wavefront_size: 64
  - .agpr_count:     0
    .args:
      - .address_space:  global
        .offset:         0
        .size:           8
        .value_kind:     global_buffer
      - .address_space:  global
        .offset:         8
        .size:           8
        .value_kind:     global_buffer
      - .actual_access:  write_only
        .address_space:  global
        .offset:         16
        .size:           8
        .value_kind:     global_buffer
      - .actual_access:  read_only
        .address_space:  global
        .offset:         24
        .size:           8
        .value_kind:     global_buffer
      - .actual_access:  read_only
        .address_space:  global
        .offset:         32
        .size:           8
        .value_kind:     global_buffer
      - .actual_access:  read_only
        .address_space:  global
        .offset:         40
        .size:           8
        .value_kind:     global_buffer
      - .actual_access:  read_only
        .address_space:  global
        .offset:         48
        .size:           8
        .value_kind:     global_buffer
      - .actual_access:  read_only
        .address_space:  global
        .offset:         56
        .size:           8
        .value_kind:     global_buffer
      - .actual_access:  read_only
        .address_space:  global
        .offset:         64
        .size:           8
        .value_kind:     global_buffer
    .group_segment_fixed_size: 98304
    .kernarg_segment_align: 8
    .kernarg_segment_size: 72
    .language:       OpenCL C
    .language_version:
      - 2
      - 0
    .max_flat_workgroup_size: 512
    .name:           _Z9gemm_gldsILi128ELi128ELi4ELi2ELi3ELi8ELi4ELi1ELi4096ELi1024ELi1024EEvPKDF16_S1_PfPKfS4_PKiPDF16_S7_S7_
    .private_segment_fixed_size: 0
    .sgpr_count:     20
    .sgpr_spill_count: 0
    .symbol:         _Z9gemm_gldsILi128ELi128ELi4ELi2ELi3ELi8ELi4ELi1ELi4096ELi1024ELi1024EEvPKDF16_S1_PfPKfS4_PKiPDF16_S7_S7_.kd
    .uniform_work_group_size: 1
    .uses_dynamic_stack: false
    .vgpr_count:     92
    .vgpr_spill_count: 0
    .wavefront_size: 64
